# NA-tail conversion point keeps converting until all 64 GLA workgroups have finished (was: until the first one)
# speedup vs baseline: 1.0182x; 1.0182x over previous
; #define LAS __attribute__((address_space(3)))
; __device__ __forceinline__ void lds_barrier() { asm volatile("s_waitcnt lgkmcnt(0)" ::: "memory"); __builtin_amdgcn_s_barrier(); asm volatile("" ::: "memory"); }
; __device__ __forceinline__ unsigned xb_add(unsigned* p, unsigned v) { return __hip_atomic_fetch_add(p, v, __ATOMIC_RELAXED, __HIP_MEMORY_SCOPE_AGENT); }
; __device__ __forceinline__ void phase_prologue(const Args& a, LAS unsigned char* lds) {
;     ...
;     unsigned* cq_head = (unsigned*)(a.ws + WS_CTL) + 8192 + 768;
;     volatile LAS int* qs = (volatile LAS int*)(lds + 128 * 129 * 4);
;     int pend = 0, it = 0;
;     if (tid == 0) { qs[0] = (int)xb_add(cq_head, 1u); pend = (int)xb_add(cq_head, 1u); }
;     __syncthreads();
;     for (int u = qs[0]; u < CTOT; u = qs[it & 1]) {
;     ...
;         const int kt = r / NT, ntl = r % NT, k0 = kt * 128, n0 = ntl * 128;
;         const int drow0 = mode == 0 ? n0 : (ntl * 256 + (mode == 2 ? 128 : 0));
;         f32x4 v[8];
; #pragma unroll
;         for (int i = 0; i < 8; ++i) { const int id = tid + 512 * i, row = id >> 5, c4 = id & 31, n = n0 + c4 * 4;
;             v[i] = (f32x4){0.f, 0.f, 0.f, 0.f};
;             if (n < nvalid) v[i] = *(const f32x4*)(src + (size_t)(k0 + row) * ldn + n); }
; #pragma unroll
;         for (int i = 0; i < 8; ++i) { const int id = tid + 512 * i, row = id >> 5, c4 = id & 31;
;             LAS float* tp = tile + row * 129 + c4 * 4; tp[0] = v[i][0]; tp[1] = v[i][1]; tp[2] = v[i][2]; tp[3] = v[i][3]; }
;         lds_barrier();
; #pragma unroll
;         for (int i = 0; i < 4; ++i) { const int piece = tid + 512 * i, nl = piece >> 4, kg = piece & 15; const LAS float* s = tile + (kg * 8) * 129 + nl;
;             u32x4 o; o.x = pk2(s[0], s[129]); o.y = pk2(s[258], s[387]); o.z = pk2(s[516], s[645]); o.w = pk2(s[774], s[903]);
;             *(u32x4*)(dst + (size_t)(drow0 + nl) * 2048 + k0 + kg * 8) = o; }
.Lcva_f0:
	s_mov_b64 exec, s[34:35]
	s_waitcnt lgkmcnt(0)
	s_barrier
	ds_read_b32 v127, v125 offset:4
	s_waitcnt lgkmcnt(0)
	v_readfirstlane_b32 s25, v127
	s_cmpk_ge_u32 s25, 0x40
	s_cbranch_scc1 .Lcva_done
	s_barrier
	v_lshrrev_b32_e32 v104, 5, v0
	v_and_b32_e32 v126, 31, v0
	v_lshlrev_b32_e32 v105, 13, v104
	v_lshl_add_u32 v105, v126, 4, v105
	v_add_u32_e32 v106, 0x20000, v105
	v_add_u32_e32 v107, 0x40000, v105
	v_add_u32_e32 v108, 0x60000, v105
	v_add_u32_e32 v109, 0x80000, v105
	v_add_u32_e32 v110, 0xa0000, v105
	v_add_u32_e32 v111, 0xc0000, v105
	v_add_u32_e32 v112, 0xe0000, v105
	v_mul_u32_u24_e32 v113, 0x204, v104
	v_lshl_add_u32 v113, v126, 4, v113
	v_lshrrev_b32_e32 v127, 4, v0
	v_and_b32_e32 v126, 15, v0
	v_mul_u32_u24_e32 v114, 0x1020, v126
	v_lshl_add_u32 v114, v127, 2, v114
	v_lshlrev_b32_e32 v115, 12, v127
	v_lshl_add_u32 v115, v126, 4, v115
	v_add_u32_e32 v116, 0x20000, v115
	v_add_u32_e32 v117, 0x40000, v115
	v_add_u32_e32 v118, 0x60000, v115
	v_readlane_b32 s42, v254, 27
	v_readlane_b32 s43, v254, 28
	s_sub_u32 s42, s42, 0x28
	s_subb_u32 s43, s43, 0
	s_load_dwordx2 s[40:41], s[42:43], 0x0
	s_waitcnt lgkmcnt(0)
	v_cmp_eq_u32_e32 vcc, 0, v0
	s_and_saveexec_b64 s[34:35], vcc
	s_cbranch_execz .Lcva_t0a
	global_atomic_add v123, v120, v119, s[94:95] sc0
	s_waitcnt vmcnt(0)
	ds_write_b32 v125, v123
	ds_write_b32 v125, v122 offset:4

; __device__ __forceinline__ void lds_barrier() { asm volatile("s_waitcnt lgkmcnt(0)" ::: "memory"); __builtin_amdgcn_s_barrier(); asm volatile("" ::: "memory"); }
; __device__ __forceinline__ unsigned xb_add(unsigned* p, unsigned v) { return __hip_atomic_fetch_add(p, v, __ATOMIC_RELAXED, __HIP_MEMORY_SCOPE_AGENT); }
; __device__ __forceinline__ void phase_prologue(const Args& a, LAS unsigned char* lds) {
;     ...
;     for (int u = qs[0]; u < CTOT; u = qs[it & 1]) {
;         int r = u; const float* src; int ldn, nvalid, NT, mode = 0; bf16_t* dst;
;     ...
;         ++it;
;         if (tid == 0) { qs[it & 1] = pend; pend = (int)xb_add(cq_head, 1u); }
;         lds_barrier();
.Lcva_loop:
	ds_read_b32 v126, v125
	ds_read_b32 v127, v125 offset:4
	s_waitcnt lgkmcnt(0)
	v_readfirstlane_b32 s24, v126
	v_readfirstlane_b32 s25, v127
	s_cmpk_gt_u32 s24, 0x1fff
	s_cbranch_scc1 .Lcva_done
	s_cmpk_ge_u32 s25, 0x40
	s_cbranch_scc1 .Lcva_nopf
	v_cmp_eq_u32_e32 vcc, 0, v0
	s_and_saveexec_b64 s[34:35], vcc
	s_cbranch_execz .Lcva_t0b
	global_atomic_add v123, v120, v119, s[94:95] sc0
	global_atomic_add v124, v121, v122, s[94:95] sc0

; #define LAS __attribute__((address_space(3)))
; __device__ __forceinline__ void lds_barrier() { asm volatile("s_waitcnt lgkmcnt(0)" ::: "memory"); __builtin_amdgcn_s_barrier(); asm volatile("" ::: "memory"); }
; __device__ __forceinline__ void phase_prologue(const Args& a, LAS unsigned char* lds) {
;     ...
;         else { r -= CJ3; const int which = r / CJM; r -= which * CJM; const int mtx = r >> 8; r &= 255; ldn = 2048; nvalid = 2048; NT = 16;
;             if (which == 0) { src = a.in[I_WGATE] + (size_t)mtx * 2048 * 2048; dst = (bf16_t*)(a.ws + WS_WGU) + (size_t)mtx * 4096 * 2048; mode = 1; }
;             else if (which == 1) { src = a.in[I_WUP] + (size_t)mtx * 2048 * 2048; dst = (bf16_t*)(a.ws + WS_WGU) + (size_t)mtx * 4096 * 2048; mode = 2; }
;             else { src = a.in[I_WDOWN] + (size_t)mtx * 2048 * 2048; dst = (bf16_t*)(a.ws + WS_WDN) + (size_t)mtx * 2048 * 2048; } }
;         const int kt = r / NT, ntl = r % NT, k0 = kt * 128, n0 = ntl * 128;
;         const int drow0 = mode == 0 ? n0 : (ntl * 256 + (mode == 2 ? 128 : 0));
;         f32x4 v[8];
; #pragma unroll
;         for (int i = 0; i < 8; ++i) { const int id = tid + 512 * i, row = id >> 5, c4 = id & 31, n = n0 + c4 * 4;
;             v[i] = (f32x4){0.f, 0.f, 0.f, 0.f};
;             if (n < nvalid) v[i] = *(const f32x4*)(src + (size_t)(k0 + row) * ldn + n); }
; #pragma unroll
;         for (int i = 0; i < 8; ++i) { const int id = tid + 512 * i, row = id >> 5, c4 = id & 31;
;             LAS float* tp = tile + row * 129 + c4 * 4; tp[0] = v[i][0]; tp[1] = v[i][1]; tp[2] = v[i][2]; tp[3] = v[i][3]; }
;         lds_barrier();
; #pragma unroll
;         for (int i = 0; i < 4; ++i) { const int piece = tid + 512 * i, nl = piece >> 4, kg = piece & 15; const LAS float* s = tile + (kg * 8) * 129 + nl;
;             u32x4 o; o.x = pk2(s[0], s[129]); o.y = pk2(s[258], s[387]); o.z = pk2(s[516], s[645]); o.w = pk2(s[774], s[903]);
;             *(u32x4*)(dst + (size_t)(drow0 + nl) * 2048 + k0 + kg * 8) = o; }
.Lcva_nopf:
	s_lshr_b32 s36, s24, 12
	s_bfe_u32 s30, s24, 0x40008
	s_add_i32 s30, s30, 16
	s_lshl_b32 s30, s30, 24
	s_bfe_u32 s31, s24, 0x40004
	s_and_b32 s32, s24, 15
	v_readlane_b32 s26, v254, 43
	v_readlane_b32 s27, v254, 44
	s_cmp_lg_u32 s36, 0
	s_cselect_b32 s26, s40, s26
	s_cselect_b32 s27, s41, s27
	s_lshl_b32 s33, s31, 20
	s_add_i32 s33, s33, s30
	s_lshl_b32 s37, s32, 9
	s_add_i32 s33, s33, s37
	s_add_u32 s26, s26, s33
	s_addc_u32 s27, s27, 0
	v_readlane_b32 s28, v254, 25
	v_readlane_b32 s29, v254, 26
	s_lshl_b32 s33, s32, 20
	s_add_i32 s33, s33, s30
	s_lshl_b32 s37, s36, 19
	s_add_i32 s33, s33, s37
	s_lshl_b32 s37, s31, 8
	s_add_i32 s33, s33, s37
	s_add_u32 s28, s28, s33
	s_addc_u32 s29, s29, 0
	global_load_dwordx4 v[128:131], v105, s[26:27]
	global_load_dwordx4 v[132:135], v106, s[26:27]
	global_load_dwordx4 v[136:139], v107, s[26:27]
	global_load_dwordx4 v[140:143], v108, s[26:27]
	global_load_dwordx4 v[144:147], v109, s[26:27]
	global_load_dwordx4 v[148:151], v110, s[26:27]
	global_load_dwordx4 v[152:155], v111, s[26:27]
	global_load_dwordx4 v[156:159], v112, s[26:27]
	s_waitcnt vmcnt(7)
	ds_write_b32 v113, v128
	ds_write_b32 v113, v129 offset:4
	ds_write_b32 v113, v130 offset:8
	ds_write_b32 v113, v131 offset:12
	s_waitcnt vmcnt(6)
	ds_write_b32 v113, v132 offset:8256
	ds_write_b32 v113, v133 offset:8260
	ds_write_b32 v113, v134 offset:8264
	ds_write_b32 v113, v135 offset:8268
	s_waitcnt vmcnt(5)
	ds_write_b32 v113, v136 offset:16512
	ds_write_b32 v113, v137 offset:16516
	ds_write_b32 v113, v138 offset:16520
	ds_write_b32 v113, v139 offset:16524
	s_waitcnt vmcnt(4)
	ds_write_b32 v113, v140 offset:24768
	ds_write_b32 v113, v141 offset:24772
	ds_write_b32 v113, v142 offset:24776
	ds_write_b32 v113, v143 offset:24780
	s_waitcnt vmcnt(3)
	ds_write_b32 v113, v144 offset:33024
	ds_write_b32 v113, v145 offset:33028
	ds_write_b32 v113, v146 offset:33032
	ds_write_b32 v113, v147 offset:33036
	s_waitcnt vmcnt(2)
	ds_write_b32 v113, v148 offset:41280
	ds_write_b32 v113, v149 offset:41284
	ds_write_b32 v113, v150 offset:41288
	ds_write_b32 v113, v151 offset:41292
	s_waitcnt vmcnt(1)
	ds_write_b32 v113, v152 offset:49536
	ds_write_b32 v113, v153 offset:49540
	ds_write_b32 v113, v154 offset:49544
	ds_write_b32 v113, v155 offset:49548
	s_waitcnt vmcnt(0)
	ds_write_b32 v113, v156 offset:57792
	ds_write_b32 v113, v157 offset:57796
	ds_write_b32 v113, v158 offset:57800
	ds_write_b32 v113, v159 offset:57804
	s_waitcnt lgkmcnt(0)
	s_barrier
	ds_read_b32 v160, v114
	ds_read_b32 v161, v114 offset:516
	ds_read_b32 v162, v114 offset:1032
	ds_read_b32 v163, v114 offset:1548
	ds_read_b32 v164, v114 offset:2064
	ds_read_b32 v165, v114 offset:2580
	ds_read_b32 v166, v114 offset:3096
	ds_read_b32 v167, v114 offset:3612
	s_waitcnt lgkmcnt(0)
	v_cvt_pk_bf16_f32 v168, v160, v161
	v_cvt_pk_bf16_f32 v169, v162, v163
	v_cvt_pk_bf16_f32 v170, v164, v165
	v_cvt_pk_bf16_f32 v171, v166, v167
	global_store_dwordx4 v115, v[168:171], s[28:29]
	ds_read_b32 v160, v114 offset:128
	ds_read_b32 v161, v114 offset:644
	ds_read_b32 v162, v114 offset:1160
	ds_read_b32 v163, v114 offset:1676
	ds_read_b32 v164, v114 offset:2192
	ds_read_b32 v165, v114 offset:2708
	ds_read_b32 v166, v114 offset:3224
	ds_read_b32 v167, v114 offset:3740
	s_waitcnt lgkmcnt(0)
	v_cvt_pk_bf16_f32 v172, v160, v161
	v_cvt_pk_bf16_f32 v173, v162, v163
	v_cvt_pk_bf16_f32 v174, v164, v165
	v_cvt_pk_bf16_f32 v175, v166, v167
	global_store_dwordx4 v116, v[172:175], s[28:29]
	ds_read_b32 v160, v114 offset:256
	ds_read_b32 v161, v114 offset:772
	ds_read_b32 v162, v114 offset:1288
	ds_read_b32 v163, v114 offset:1804
	ds_read_b32 v164, v114 offset:2320
	ds_read_b32 v165, v114 offset:2836
	ds_read_b32 v166, v114 offset:3352
	ds_read_b32 v167, v114 offset:3868
	s_waitcnt lgkmcnt(0)
	v_cvt_pk_bf16_f32 v168, v160, v161
	v_cvt_pk_bf16_f32 v169, v162, v163
	v_cvt_pk_bf16_f32 v170, v164, v165
	v_cvt_pk_bf16_f32 v171, v166, v167
	global_store_dwordx4 v117, v[168:171], s[28:29]
	ds_read_b32 v160, v114 offset:384
	ds_read_b32 v161, v114 offset:900
	ds_read_b32 v162, v114 offset:1416
	ds_read_b32 v163, v114 offset:1932
	ds_read_b32 v164, v114 offset:2448
	ds_read_b32 v165, v114 offset:2964
	ds_read_b32 v166, v114 offset:3480
	ds_read_b32 v167, v114 offset:3996
	s_waitcnt lgkmcnt(0)
	v_cvt_pk_bf16_f32 v172, v160, v161
	v_cvt_pk_bf16_f32 v173, v162, v163
	v_cvt_pk_bf16_f32 v174, v164, v165
	v_cvt_pk_bf16_f32 v175, v166, v167
	global_store_dwordx4 v118, v[172:175], s[28:29]
	s_cmpk_ge_u32 s25, 0x40
	s_cbranch_scc1 .Lcva_done
	v_cmp_eq_u32_e32 vcc, 0, v0
	s_and_saveexec_b64 s[34:35], vcc
	s_cbranch_execz .Lcva_t0c
	s_waitcnt vmcnt(0)
	ds_write_b32 v125, v123
	ds_write_b32 v125, v124 offset:4
